# baseline (speedup 1.0000x reference)
_Z10qkv_kernelN3pg84GemmENS_7EpiRopeEN2hg4GemmENS2_7EpiRopeE:
	s_getpc_b64 s[94:95]
	s_load_dwordx4 s[4:7], s[0:1], 0x10
	s_load_dword s33, s[0:1], 0x30
	s_load_dwordx4 s[8:11], s[0:1], 0x48
	s_load_dwordx2 s[28:29], s[0:1], 0x68
	v_readfirstlane_b32 s53, v0
	s_waitcnt lgkmcnt(0)
	s_ashr_i32 s3, s4, 31
	s_lshr_b32 s3, s3, 24
	s_add_i32 s3, s4, s3
	s_ashr_i32 s52, s3, 8
	s_ashr_i32 s3, s5, 31
	s_lshr_b32 s3, s3, 24
	s_add_i32 s3, s5, s3
	s_ashr_i32 s40, s3, 8
	s_mul_i32 s4, s40, s52
	s_cmp_ge_i32 s2, s4
	s_cselect_b64 s[30:31], -1, 0
	s_and_b64 vcc, exec, s[30:31]
	s_cbranch_vccnz .LBB1_6
	s_ashr_i32 s3, s4, 31
	s_lshr_b32 s3, s3, 29
	s_add_i32 s3, s4, s3
	s_ashr_i32 s5, s3, 3
	s_and_b32 s3, s3, -8
	s_sub_i32 s12, s4, s3
	s_ashr_i32 s3, s2, 31
	s_lshr_b32 s3, s3, 29
	s_add_i32 s3, s2, s3
	s_and_b32 s7, s3, -8
	s_sub_i32 s7, s2, s7
	s_add_i32 s11, s5, 1
	s_cmp_ge_i32 s7, s12
	s_cbranch_scc0 .LBB1_3
	s_mul_i32 s13, s11, s12
	s_sub_i32 s12, s7, s12
	s_mul_i32 s5, s12, s5
	s_add_i32 s5, s5, s13
	s_cbranch_execz .LBB1_4
	s_branch .LBB1_5

.LBB1_9:
	v_lshrrev_b32_e32 v171, 1, v2
	v_or_b32_e32 v176, v18, v16
	v_and_or_b32 v175, v5, 32, v3
	v_or_b32_e32 v174, v17, v16
	v_and_or_b32 v172, v6, s5, v3
	v_and_b32_e32 v168, 15, v0
	v_lshlrev_b32_e32 v170, 3, v1
	s_andn2_b64 vcc, exec, s[0:1]
	v_bitop3_b32 v173, v169, v7, v4 bitop3:0x36
	s_cbranch_vccnz .LBB1_208
	s_ashr_i32 s7, s6, 31
	s_lshl_b64 s[34:35], s[6:7], 9
	s_ashr_i32 s5, s80, 31
	s_mul_i32 s5, s34, s5
	s_mul_hi_u32 s36, s34, s80
	s_ashr_i32 s38, s79, 31
	s_add_i32 s5, s36, s5
	s_lshr_b64 s[36:37], s[6:7], 23
	s_mul_i32 s38, s34, s38
	s_mul_hi_u32 s39, s34, s79
	s_lshr_b32 s0, s53, 6
	s_mul_i32 s37, s36, s80
	s_add_i32 s38, s39, s38
	s_mul_i32 s36, s36, s79
	s_lshr_b32 s1, s53, 8
	s_lshl_b64 s[30:31], s[6:7], 8
	s_lshl_b32 s56, s0, 10
	s_add_i32 s5, s5, s37
	s_add_i32 s38, s38, s36
	s_mul_i32 s36, s34, s79
	v_mul_lo_u32 v2, s6, v176
	s_waitcnt lgkmcnt(0)
	s_lshr_b32 s93, s2, 3
	s_lshl_b32 s93, s93, 3
	s_or_b32 s93, s93, s0
	s_lshl_b32 s93, s93, 7
	s_cmp_lt_u32 s93, 0x5200
	s_cbranch_scc0 .Lpfq_skip
	s_add_u32 s94, s94, s93
	s_addc_u32 s95, s95, 0
	s_load_dword s93, s[94:95], 0x0
	s_load_dword s93, s[94:95], 0x40
.Lpfq_skip:
	s_add_u32 s44, s26, s36
	v_add_lshl_u32 v146, v2, v171, 1
	v_mul_lo_u32 v2, s6, v175
	s_addc_u32 s45, s27, s38
	s_add_i32 s57, s56, 0
	v_add_lshl_u32 v148, v2, v171, 1
	v_mul_lo_u32 v2, s6, v174
	s_add_i32 m0, s57, 0x10000
	v_add_lshl_u32 v150, v2, v171, 1
	v_mul_lo_u32 v2, s6, v172
	s_mul_i32 s37, s34, s80
	global_load_lds_dwordx4 v148, s[44:45]
	s_add_i32 m0, s57, 0x12000
	v_add_lshl_u32 v152, v2, v171, 1
	s_add_u32 s46, s24, s37
	global_load_lds_dwordx4 v152, s[44:45]
	s_addc_u32 s47, s25, s5
	s_mov_b32 m0, s57
	s_add_i32 s58, s57, 0x2000
	global_load_lds_dwordx4 v146, s[46:47]
	s_mov_b32 m0, s58
	s_add_u32 s36, s44, s30
	global_load_lds_dwordx4 v150, s[46:47]
	s_addc_u32 s37, s45, s31
	s_add_i32 m0, s57, 0x14000
	v_mov_b32_e32 v67, 0
	global_load_lds_dwordx4 v148, s[36:37]
	s_add_i32 m0, s57, 0x16000
	s_add_u32 s38, s46, s30
	s_addc_u32 s39, s47, s31
	s_add_i32 s59, s57, 0x4000
	global_load_lds_dwordx4 v152, s[36:37]
	s_mov_b32 m0, s59
	s_add_i32 s60, s57, 0x6000
	global_load_lds_dwordx4 v146, s[38:39]
	s_mov_b32 m0, s60
	v_mov_b32_e32 v149, v67
	global_load_lds_dwordx4 v150, s[38:39]
	v_mov_b32_e32 v153, v67
	v_mov_b32_e32 v147, v67
	v_mov_b32_e32 v151, v67
	s_mov_b32 s81, 0
	v_lshl_add_u64 v[12:13], s[44:45], 0, v[148:149]
	v_lshl_add_u64 v[10:11], s[44:45], 0, v[152:153]
	v_lshl_add_u64 v[8:9], s[46:47], 0, v[146:147]
	v_lshl_add_u64 v[6:7], s[46:47], 0, v[150:151]
	v_lshl_add_u64 v[4:5], s[36:37], 0, v[148:149]
	s_cmp_lg_u32 s1, 1
	v_lshl_add_u64 v[2:3], s[36:37], 0, v[152:153]
	s_cbranch_scc1 .LBB1_12
	s_barrier

	.amdhsa_kernel _Z10qkv_kernelN3pg84GemmENS_7EpiRopeEN2hg4GemmENS2_7EpiRopeE
		.amdhsa_group_segment_fixed_size 0
		.amdhsa_private_segment_fixed_size 0
		.amdhsa_kernarg_size 368
		.amdhsa_user_sgpr_count 2
		.amdhsa_user_sgpr_dispatch_ptr 0
		.amdhsa_user_sgpr_queue_ptr 0
		.amdhsa_user_sgpr_kernarg_segment_ptr 1
		.amdhsa_user_sgpr_dispatch_id 0
		.amdhsa_user_sgpr_kernarg_preload_length 0
		.amdhsa_user_sgpr_kernarg_preload_offset 0
		.amdhsa_user_sgpr_private_segment_size 0
		.amdhsa_uses_dynamic_stack 0
		.amdhsa_enable_private_segment 0
		.amdhsa_system_sgpr_workgroup_id_x 1
		.amdhsa_system_sgpr_workgroup_id_y 0
		.amdhsa_system_sgpr_workgroup_id_z 0
		.amdhsa_system_sgpr_workgroup_info 0
		.amdhsa_system_vgpr_workitem_id 0
		.amdhsa_next_free_vgpr 240
		.amdhsa_next_free_sgpr 96
		.amdhsa_accum_offset 240
		.amdhsa_reserve_vcc 1
		.amdhsa_float_round_mode_32 0
		.amdhsa_float_round_mode_16_64 0
		.amdhsa_float_denorm_mode_32 3
		.amdhsa_float_denorm_mode_16_64 3
		.amdhsa_dx10_clamp 1
		.amdhsa_ieee_mode 1
		.amdhsa_fp16_overflow 0
		.amdhsa_tg_split 0
		.amdhsa_exception_fp_ieee_invalid_op 0
		.amdhsa_exception_fp_denorm_src 0
		.amdhsa_exception_fp_ieee_div_zero 0
		.amdhsa_exception_fp_ieee_overflow 0
		.amdhsa_exception_fp_ieee_underflow 0
		.amdhsa_exception_fp_ieee_inexact 0
		.amdhsa_exception_int_div_zero 0
	.end_amdhsa_kernel

_Z11attn_kernelPKDF16_S0_S0_PDF16_:
	s_getpc_b64 s[52:53]
	s_bfe_u32 s26, s2, 0x20003
	s_load_dwordx8 s[4:11], s[0:1], 0x0
	s_lshr_b32 s1, s2, 2
	s_lshr_b32 s20, s2, 6
	v_readfirstlane_b32 s19, v0
	s_mov_b32 s21, 0
	s_lshl_b32 s27, s26, 8
	s_and_b32 s0, s2, 7
	s_and_b32 s1, s1, 8
	s_lshr_b32 s34, s19, 6
	s_lshr_b32 s55, s19, 6
	s_lshr_b32 s54, s2, 3
	s_lshl_b32 s54, s54, 3
	s_or_b32 s54, s54, s55
	s_lshl_b32 s54, s54, 7
	s_add_u32 s52, s52, s54
	s_addc_u32 s53, s53, 0
	s_lshl_b64 s[12:13], s[20:21], 11
	s_xor_b32 s16, s27, 0x700
	s_or_b32 s18, s1, s0
	s_or_b32 s0, s12, s16
	s_lshl_b32 s24, s34, 5
	s_add_u32 s0, s0, s24
	s_addc_u32 s1, s13, 0
	s_lshl_b64 s[14:15], s[0:1], 10
	s_lshl_b64 s[0:1], s[0:1], 11
	s_waitcnt lgkmcnt(0)
	s_cmp_lt_u32 s54, 0x7000
	s_cbranch_scc0 .Lpfa_skip
	s_load_dword s54, s[52:53], 0x0
	s_load_dword s54, s[52:53], 0x40
.Lpfa_skip:
	s_add_u32 s0, s4, s0
	s_addc_u32 s1, s5, s1
	s_lshl_b32 s33, s18, 6
	s_lshl_b32 s2, s18, 7
	s_add_u32 s2, s0, s2
	s_addc_u32 s3, s1, 0
	s_lshl_b32 s0, s20, 4
	s_or_b32 s20, s18, s0
	s_and_b32 s17, s19, 0x3fffffc0
	s_lshl_b64 s[0:1], s[20:21], 18
	s_add_u32 s28, s6, s0
	s_addc_u32 s29, s7, s1
	s_lshl_b32 s18, s34, 10
	s_add_u32 s6, s28, s18
	s_addc_u32 s7, s29, 0
	s_add_u32 s30, s8, s0
	s_addc_u32 s31, s9, s1
	s_lshl_b32 s0, s19, 4
	v_and_b32_e32 v207, 63, v0
	s_and_b32 s0, s0, 0xfffff000
	v_mov_b32_e32 v3, 0
	v_lshlrev_b32_e32 v2, 4, v207
	s_add_u32 s0, s30, s0
	v_lshl_add_u64 v[212:213], s[6:7], 0, v[2:3]
	s_addc_u32 s1, s31, 0
	s_lshr_b32 s6, s19, 2
	v_bfe_u32 v1, v0, 2, 4
	v_and_or_b32 v2, s6, 48, v1
	v_lshlrev_b32_e32 v2, 6, v2
	v_lshlrev_b32_e32 v209, 3, v0
	s_cmp_lg_u32 0, -1
	v_lshl_add_u64 v[4:5], s[0:1], 0, v[2:3]
	v_and_b32_e32 v208, 24, v209
	s_cselect_b32 s0, 0, 0
	v_and_b32_e32 v222, 31, v0
	v_lshlrev_b32_e32 v2, 1, v208
	s_add_i32 s35, s18, s0
	s_mov_b32 s0, m0
	s_mov_b32 m0, s35
	s_nop 0
	global_load_lds_dwordx4 v[212:213], off
	s_mov_b32 m0, s0
	v_bfe_u32 v211, v0, 5, 1
	v_lshl_add_u64 v[194:195], v[4:5], 0, v[2:3]
	s_add_i32 s39, s35, 0x6000
	s_mov_b32 s0, m0
	s_mov_b32 m0, s39
	s_nop 0
	global_load_lds_dwordx4 v[194:195], off
	s_mov_b32 m0, s0
	v_lshlrev_b32_e32 v2, 10, v222
	s_mov_b64 s[0:1], 0x2000
	v_lshl_or_b32 v210, v211, 3, v2
	v_lshl_add_u64 v[214:215], v[212:213], 0, s[0:1]
	s_add_i32 s36, s35, 0x2000
	s_mov_b32 s6, m0
	s_mov_b32 m0, s36
	s_nop 0
	global_load_lds_dwordx4 v[214:215], off
	s_mov_b32 m0, s6
	v_lshlrev_b32_e32 v2, 1, v210
	global_load_dwordx4 v[158:161], v2, s[2:3]
	global_load_dwordx4 v[154:157], v2, s[2:3] offset:32
	global_load_dwordx4 v[150:153], v2, s[2:3] offset:64
	global_load_dwordx4 v[146:149], v2, s[2:3] offset:96
	v_lshlrev_b32_e32 v4, 10, v211
	v_lshlrev_b32_e32 v5, 4, v222
	v_add3_u32 v224, 0, v4, v5
	v_mov_b32_e32 v4, v3
	v_mov_b32_e32 v5, v3
	v_mov_b32_e32 v6, v3
	v_mov_b32_e32 v7, v3
	v_mov_b32_e32 v8, v3
	v_mov_b32_e32 v9, v3
	v_mov_b32_e32 v10, v3
	v_mov_b32_e32 v11, v3
	v_mov_b32_e32 v12, v3
	v_mov_b32_e32 v13, v3
	v_mov_b32_e32 v14, v3
	v_mov_b32_e32 v15, v3
	v_mov_b32_e32 v16, v3
	v_mov_b32_e32 v17, v3
	v_mov_b32_e32 v18, v3
	v_mov_b32_e32 v19, v3
	s_mov_b64 s[2:3], 0x4000
	s_add_i32 s37, s35, 0x4000
	v_lshl_add_u64 v[216:217], v[212:213], 0, s[2:3]
	s_mov_b32 s6, m0
	s_mov_b32 m0, s37
	s_nop 0
	global_load_lds_dwordx4 v[216:217], off
	s_mov_b32 m0, s6
	s_waitcnt vmcnt(3) lgkmcnt(0)
	s_barrier
	ds_read_b128 v[36:39], v224
	ds_read_b128 v[40:43], v224 offset:512
	s_mov_b64 s[6:7], 0x6000
	s_mov_b32 s41, 3
	s_movk_i32 s46, 0x2000
	s_movk_i32 s25, 0x4000
	s_sub_i32 s43, 0xbf, s16
	s_mov_b32 s45, 0x41000000
	s_mov_b64 s[18:19], 0xa000
	v_lshlrev_b32_e32 v226, 4, v211
	v_mov_b32_e32 v233, v3
	v_lshlrev_b32_e32 v206, 3, v207
	s_waitcnt vmcnt(3) lgkmcnt(1)
	v_mfma_f32_32x32x16_f16 v[20:35], v[36:39], v[158:161], v[4:19]
	s_waitcnt lgkmcnt(0)
	v_mfma_f32_32x32x16_f16 v[4:19], v[40:43], v[158:161], v[4:19]
	ds_read_b128 v[36:39], v224 offset:2048
	ds_read_b128 v[40:43], v224 offset:2560
	s_waitcnt vmcnt(2) lgkmcnt(1)
	v_mfma_f32_32x32x16_f16 v[20:35], v[36:39], v[154:157], v[20:35]
	s_waitcnt lgkmcnt(0)
	v_mfma_f32_32x32x16_f16 v[4:19], v[40:43], v[154:157], v[4:19]
	ds_read_b128 v[36:39], v224 offset:4096
	ds_read_b128 v[40:43], v224 offset:4608
	s_waitcnt vmcnt(1) lgkmcnt(1)
	v_mfma_f32_32x32x16_f16 v[20:35], v[36:39], v[150:153], v[20:35]
	s_waitcnt lgkmcnt(0)
	v_mfma_f32_32x32x16_f16 v[4:19], v[40:43], v[150:153], v[4:19]
	ds_read_b128 v[36:39], v224 offset:6144
	ds_read_b128 v[40:43], v224 offset:6656
	s_waitcnt vmcnt(0) lgkmcnt(1)
	v_mfma_f32_32x32x16_f16 v[20:35], v[36:39], v[146:149], v[20:35]
	s_waitcnt lgkmcnt(0)
	v_mfma_f32_32x32x16_f16 v[4:19], v[40:43], v[146:149], v[4:19]
	s_nop 15
	s_nop 7
	s_nop 0
	v_max3_f32 v2, v20, v21, v4
	v_max3_f32 v36, v22, v23, v5
	s_nop 0
	v_max3_f32 v2, v2, v6, v7
	v_max3_f32 v36, v36, v26, v27
	s_nop 0
	v_max3_f32 v2, v2, v24, v25
	v_max3_f32 v36, v36, v10, v11
	s_nop 0
	v_max3_f32 v2, v2, v8, v9
	v_max3_f32 v36, v36, v30, v31
	s_nop 0
	v_max3_f32 v2, v2, v28, v29
	v_max3_f32 v36, v36, v14, v15
	s_nop 0
	v_max3_f32 v2, v2, v12, v13
	v_max3_f32 v36, v36, v34, v35
	s_nop 0
	v_max3_f32 v2, v2, v32, v33
	v_max3_f32 v36, v36, v18, v19
	s_nop 0
	v_max3_f32 v2, v2, v16, v17
	s_nop 0
	v_max_f32_e32 v2, v2, v36
	s_nop 0
	v_mov_b32_e32 v36, v2
	s_nop 1
	v_permlane32_swap_b32_e32 v2, v36
	v_max_f32_e32 v2, v2, v36
	s_nop 0
	v_sub_f32_e32 v50, v34, v2
	v_add_f32_e32 v231, v3, v2
	v_sub_f32_e32 v51, v35, v2
	v_sub_f32_e32 v52, v4, v2
	v_sub_f32_e32 v53, v5, v2
	v_lshl_add_u64 v[4:5], v[212:213], 0, s[6:7]
	v_xor_b32_e32 v34, 0x80000000, v231
	v_mov_b32_e32 v35, v34
	v_mov_b32_e32 v36, v34
	v_mov_b32_e32 v37, v34
	v_mov_b32_e32 v38, v34
	v_mov_b32_e32 v39, v34
	v_mov_b32_e32 v40, v34
	v_mov_b32_e32 v41, v34
	v_mov_b32_e32 v42, v34
	v_mov_b32_e32 v43, v34
	v_mov_b32_e32 v44, v34
	v_mov_b32_e32 v45, v34
	v_mov_b32_e32 v46, v34
	v_mov_b32_e32 v47, v34
	v_mov_b32_e32 v48, v34
	v_mov_b32_e32 v49, v34
	s_waitcnt vmcnt(0) lgkmcnt(0)
	s_barrier
	s_mov_b32 s8, m0
	s_mov_b32 m0, s35
	s_nop 0
	global_load_lds_dwordx4 v[4:5], off
	s_mov_b32 m0, s8
	s_add_i32 s8, s35, 0x8000
	v_lshl_add_u64 v[4:5], v[194:195], 0, s[0:1]
	s_mov_b32 s0, m0
	s_mov_b32 m0, s8
	s_nop 0
	global_load_lds_dwordx4 v[4:5], off
	s_mov_b32 m0, s0
	ds_read_b128 v[190:193], v224 offset:8192
	ds_read_b128 v[186:189], v224 offset:8704
	ds_read_b128 v[182:185], v224 offset:10240
	ds_read_b128 v[178:181], v224 offset:10752
	ds_read_b128 v[174:177], v224 offset:12288
	ds_read_b128 v[170:173], v224 offset:12800
	ds_read_b128 v[166:169], v224 offset:14336
	ds_read_b128 v[162:165], v224 offset:14848
	v_sub_f32_e32 v20, v20, v2
	v_sub_f32_e32 v21, v21, v2
	v_sub_f32_e32 v22, v22, v2
	v_sub_f32_e32 v23, v23, v2
	v_sub_f32_e32 v24, v24, v2
	v_sub_f32_e32 v25, v25, v2
	v_sub_f32_e32 v26, v26, v2
	v_sub_f32_e32 v27, v27, v2
	v_sub_f32_e32 v28, v28, v2
	v_sub_f32_e32 v29, v29, v2
	v_sub_f32_e32 v30, v30, v2
	v_sub_f32_e32 v31, v31, v2
	v_sub_f32_e32 v32, v32, v2
	v_sub_f32_e32 v33, v33, v2
	v_sub_f32_e32 v6, v6, v2
	v_sub_f32_e32 v7, v7, v2
	v_sub_f32_e32 v8, v8, v2
	v_sub_f32_e32 v9, v9, v2
	v_sub_f32_e32 v10, v10, v2
	v_sub_f32_e32 v11, v11, v2
	v_sub_f32_e32 v12, v12, v2
	v_sub_f32_e32 v13, v13, v2
	v_sub_f32_e32 v14, v14, v2
	v_sub_f32_e32 v15, v15, v2
	v_sub_f32_e32 v16, v16, v2
	v_sub_f32_e32 v17, v17, v2
	v_sub_f32_e32 v18, v18, v2
	v_sub_f32_e32 v19, v19, v2
	v_lshlrev_b32_e32 v2, 1, v0
	v_and_b32_e32 v228, 32, v2
	v_lshlrev_b32_e32 v2, 4, v0
	v_exp_f32_e32 v81, v51
	v_exp_f32_e32 v66, v20
	v_exp_f32_e32 v67, v21
	v_exp_f32_e32 v68, v22
	v_exp_f32_e32 v69, v23
	v_exp_f32_e32 v70, v24
	v_exp_f32_e32 v71, v25
	v_exp_f32_e32 v72, v26
	v_exp_f32_e32 v73, v27
	v_exp_f32_e32 v74, v28
	v_exp_f32_e32 v75, v29
	v_exp_f32_e32 v76, v30
	v_exp_f32_e32 v77, v31
	v_exp_f32_e32 v78, v32
	v_exp_f32_e32 v79, v33
	v_exp_f32_e32 v80, v50
	v_exp_f32_e32 v65, v19
	v_exp_f32_e32 v50, v52
	v_exp_f32_e32 v51, v53
	v_exp_f32_e32 v52, v6
	v_exp_f32_e32 v53, v7
	v_exp_f32_e32 v54, v8
	v_exp_f32_e32 v55, v9
	v_exp_f32_e32 v56, v10
	v_exp_f32_e32 v57, v11
	v_exp_f32_e32 v58, v12
	v_exp_f32_e32 v59, v13
	v_exp_f32_e32 v60, v14
	v_exp_f32_e32 v61, v15
	v_exp_f32_e32 v62, v16
	v_exp_f32_e32 v63, v17
	v_exp_f32_e32 v64, v18
	v_and_b32_e32 v2, 0xc0, v2
	s_add_i32 s0, s16, 0x100
	v_lshl_or_b32 v230, v211, 8, v2
	v_add_u32_e32 v2, 0, v228
	v_mov_b32_e32 v16, v3
	v_mov_b32_e32 v17, v3
	s_lshr_b32 s42, s0, 6
	s_lshl_b32 s0, s17, 2
	s_waitcnt vmcnt(2) lgkmcnt(0)
	s_barrier
	v_add3_u32 v225, v2, v208, v230
	v_mov_b32_e32 v2, v3
	v_mov_b32_e32 v4, v3
	v_mov_b32_e32 v5, v3
	v_mov_b32_e32 v6, v3
	v_mov_b32_e32 v7, v3
	v_mov_b32_e32 v8, v3
	v_mov_b32_e32 v9, v3
	v_mov_b32_e32 v10, v3
	v_mov_b32_e32 v11, v3
	v_mov_b32_e32 v12, v3
	v_mov_b32_e32 v13, v3
	v_mov_b32_e32 v14, v3
	v_mov_b32_e32 v15, v3
	s_add_i32 s38, s0, 0
	v_mov_b64_e32 v[32:33], v[16:17]
	v_cmp_gt_u32_e64 s[0:1], 32, v207
	s_mov_b64 s[8:9], 0
	s_mov_b64 s[16:17], 0x8000
	v_lshl_add_u32 v223, v222, 2, s38
	v_mov_b64_e32 v[30:31], v[14:15]
	v_mov_b64_e32 v[28:29], v[12:13]
	v_mov_b64_e32 v[26:27], v[10:11]
	v_mov_b64_e32 v[24:25], v[8:9]
	v_mov_b64_e32 v[22:23], v[6:7]
	v_mov_b64_e32 v[20:21], v[4:5]
	v_mov_b64_e32 v[18:19], v[2:3]

amdhsa.kernels:
  - .agpr_count:     0
    .args:
      - .actual_access:  read_only
        .address_space:  global
        .offset:         0
        .size:           8
        .value_kind:     global_buffer
      - .actual_access:  read_only
        .address_space:  global
        .offset:         8
        .size:           8
        .value_kind:     global_buffer
      - .actual_access:  read_only
        .address_space:  global
        .offset:         16
        .size:           8
        .value_kind:     global_buffer
      - .actual_access:  read_only
        .address_space:  global
        .offset:         24
        .size:           8
        .value_kind:     global_buffer
      - .actual_access:  read_only
        .address_space:  global
        .offset:         32
        .size:           8
        .value_kind:     global_buffer
      - .actual_access:  read_only
        .address_space:  global
        .offset:         40
        .size:           8
        .value_kind:     global_buffer
      - .address_space:  global
        .offset:         48
        .size:           8
        .value_kind:     global_buffer
      - .address_space:  global
        .offset:         56
        .size:           8
        .value_kind:     global_buffer
      - .address_space:  global
        .offset:         64
        .size:           8
        .value_kind:     global_buffer
      - .address_space:  global
        .offset:         72
        .size:           8
        .value_kind:     global_buffer
    .group_segment_fixed_size: 0
    .kernarg_segment_align: 8
    .kernarg_segment_size: 80
    .language:       OpenCL C
    .language_version:
      - 2
      - 0
    .max_flat_workgroup_size: 256
    .name:           _Z11prep_kernelPKfPKiS0_S0_S0_S0_PtS3_S3_P15HIP_vector_typeIfLj2EE
    .private_segment_fixed_size: 0
    .sgpr_count:     44
    .sgpr_spill_count: 0
    .symbol:         _Z11prep_kernelPKfPKiS0_S0_S0_S0_PtS3_S3_P15HIP_vector_typeIfLj2EE.kd
    .uniform_work_group_size: 1
    .uses_dynamic_stack: false
    .vgpr_count:     40
    .vgpr_spill_count: 0
    .wavefront_size: 64
  - .agpr_count:     0
    .args:
      - .offset:         0
        .size:           32
        .value_kind:     by_value
      - .offset:         32
        .size:           24
        .value_kind:     by_value
      - .offset:         56
        .size:           32
        .value_kind:     by_value
      - .offset:         88
        .size:           24
        .value_kind:     by_value
      - .offset:         112
        .size:           4
        .value_kind:     hidden_block_count_x
      - .offset:         116
        .size:           4
        .value_kind:     hidden_block_count_y
      - .offset:         120
        .size:           4
        .value_kind:     hidden_block_count_z
      - .offset:         124
        .size:           2
        .value_kind:     hidden_group_size_x
      - .offset:         126
        .size:           2
        .value_kind:     hidden_group_size_y
      - .offset:         128
        .size:           2
        .value_kind:     hidden_group_size_z
      - .offset:         130
        .size:           2
        .value_kind:     hidden_remainder_x
      - .offset:         132
        .size:           2
        .value_kind:     hidden_remainder_y
      - .offset:         134
        .size:           2
        .value_kind:     hidden_remainder_z
      - .offset:         152
        .size:           8
        .value_kind:     hidden_global_offset_x
      - .offset:         160
        .size:           8
        .value_kind:     hidden_global_offset_y
      - .offset:         168
        .size:           8
        .value_kind:     hidden_global_offset_z
      - .offset:         176
        .size:           2
        .value_kind:     hidden_grid_dims
      - .offset:         232
        .size:           4
        .value_kind:     hidden_dynamic_lds_size
    .group_segment_fixed_size: 0
    .kernarg_segment_align: 8
    .kernarg_segment_size: 368
    .language:       OpenCL C
    .language_version:
      - 2
      - 0
    .max_flat_workgroup_size: 512
    .name:           _Z10qkv_kernelN3pg84GemmENS_7EpiRopeEN2hg4GemmENS2_7EpiRopeE
    .private_segment_fixed_size: 0
    .sgpr_count:     102
    .sgpr_spill_count: 0
    .symbol:         _Z10qkv_kernelN3pg84GemmENS_7EpiRopeEN2hg4GemmENS2_7EpiRopeE.kd
    .uniform_work_group_size: 1
    .uses_dynamic_stack: false
    .vgpr_count:     240
    .vgpr_spill_count: 0
    .wavefront_size: 64
  - .agpr_count:     0
    .args:
      - .address_space:  global
        .offset:         0
        .size:           8
        .value_kind:     global_buffer
      - .address_space:  global
        .offset:         8
        .size:           8
        .value_kind:     global_buffer
      - .address_space:  global
        .offset:         16
        .size:           8
        .value_kind:     global_buffer
      - .address_space:  global
        .offset:         24
        .size:           8
        .value_kind:     global_buffer
    .group_segment_fixed_size: 0
    .kernarg_segment_align: 8
    .kernarg_segment_size: 32
    .language:       OpenCL C
    .language_version:
      - 2
      - 0
    .max_flat_workgroup_size: 512
    .name:           _Z11attn_kernelPKDF16_S0_S0_PDF16_
    .private_segment_fixed_size: 0
    .sgpr_count:     62
    .sgpr_spill_count: 0
    .symbol:         _Z11attn_kernelPKDF16_S0_S0_PDF16_.kd
    .uniform_work_group_size: 1
    .uses_dynamic_stack: false
    .vgpr_count:     243
    .vgpr_spill_count: 0
    .wavefront_size: 64
  - .agpr_count:     0
    .args:
      - .offset:         0
        .size:           32
        .value_kind:     by_value
      - .offset:         32
        .size:           16
        .value_kind:     by_value
      - .offset:         48
        .size:           4
        .value_kind:     hidden_block_count_x
      - .offset:         52
        .size:           4
        .value_kind:     hidden_block_count_y
      - .offset:         56
        .size:           4
        .value_kind:     hidden_block_count_z
      - .offset:         60
        .size:           2
        .value_kind:     hidden_group_size_x
      - .offset:         62
        .size:           2
        .value_kind:     hidden_group_size_y
      - .offset:         64
        .size:           2
        .value_kind:     hidden_group_size_z
      - .offset:         66
        .size:           2
        .value_kind:     hidden_remainder_x
      - .offset:         68
        .size:           2
        .value_kind:     hidden_remainder_y
      - .offset:         70
        .size:           2
        .value_kind:     hidden_remainder_z
      - .offset:         88
        .size:           8
        .value_kind:     hidden_global_offset_x
      - .offset:         96
        .size:           8
        .value_kind:     hidden_global_offset_y
      - .offset:         104
        .size:           8
        .value_kind:     hidden_global_offset_z
      - .offset:         112
        .size:           2
        .value_kind:     hidden_grid_dims
      - .offset:         168
        .size:           4
        .value_kind:     hidden_dynamic_lds_size
    .group_segment_fixed_size: 0
    .kernarg_segment_align: 8
    .kernarg_segment_size: 304
    .language:       OpenCL C
    .language_version:
      - 2
      - 0
    .max_flat_workgroup_size: 512
    .name:           _Z12hgemm_kernelIN2hg6EpiF32EEvNS0_4GemmET_
    .private_segment_fixed_size: 0
    .sgpr_count:     62
    .sgpr_spill_count: 0
    .symbol:         _Z12hgemm_kernelIN2hg6EpiF32EEvNS0_4GemmET_.kd
    .uniform_work_group_size: 1
    .uses_dynamic_stack: false
    .vgpr_count:     138
    .vgpr_spill_count: 0
    .wavefront_size: 64
